# combined: attention DMA-issue trims + carried ring indices + redundant post-barrier waits removed in GEMM loops, on top of the MFMA-first attention heads
# speedup vs baseline: 1.0045x; 1.0045x over previous
.LBB0_1319:
	v_mfma_f32_32x32x16_bf16 v[82:97], v[138:141], v[98:101], 0
	v_lshl_add_u32 v162, s90, 13, v240
	ds_read_b64_tr_b16 v[142:143], v162 offset:40960
	ds_read_b64_tr_b16 v[144:145], v162 offset:41472
	s_add_i32 s45, s44, -1
	v_add_f32_e32 v66, v50, v51
	v_add_f32_e32 v67, v52, v53
	v_add_f32_e32 v66, v66, v67
	v_cvt_pk_bf16_f32 v138, v50, v51
	v_cvt_pk_bf16_f32 v139, v52, v53
	ds_read_b64_tr_b16 v[146:147], v162 offset:45056
	ds_read_b64_tr_b16 v[148:149], v162 offset:45568
	v_add_f32_e32 v50, v54, v55
	v_add_f32_e32 v51, v56, v57
	v_add_f32_e32 v50, v50, v51
	v_add_f32_e32 v50, v50, v66
	v_mfma_f32_32x32x16_bf16 v[66:81], v[130:133], v[98:101], 0
	v_cvt_pk_bf16_f32 v140, v54, v55
	v_cvt_pk_bf16_f32 v141, v56, v57
	v_add_u32_e32 v150, s98, v238
	ds_read_b128 v[130:133], v150 offset:6144
	ds_read_b128 v[158:161], v150 offset:6656
	ds_read_b64_tr_b16 v[54:55], v162 offset:41984
	ds_read_b64_tr_b16 v[56:57], v162 offset:42496
	v_mfma_f32_32x32x16_bf16 v[82:97], v[134:137], v[102:105], v[82:97]
	v_add_f32_e32 v51, v58, v59
	v_add_f32_e32 v52, v60, v61
	v_add_f32_e32 v51, v51, v52
	v_add_f32_e32 v52, v51, v50
	v_cvt_pk_bf16_f32 v50, v58, v59
	v_cvt_pk_bf16_f32 v51, v60, v61
	ds_read_b64_tr_b16 v[58:59], v162 offset:46080
	ds_read_b64_tr_b16 v[60:61], v162 offset:46592
	v_mfma_f32_32x32x16_bf16 v[66:81], v[126:129], v[102:105], v[66:81]
	v_add_f32_e32 v53, v62, v63
	v_add_f32_e32 v126, v64, v65
	v_add_f32_e32 v53, v53, v126
	v_add_f32_e32 v151, v53, v52
	v_cvt_pk_bf16_f32 v52, v62, v63
	v_cvt_pk_bf16_f32 v53, v64, v65
	ds_read_b128 v[126:129], v150 offset:8192
	ds_read_b128 v[134:137], v150 offset:8704
	ds_read_b64_tr_b16 v[62:63], v162 offset:43008
	ds_read_b64_tr_b16 v[64:65], v162 offset:43520
	v_mfma_f32_32x32x16_bf16 v[82:97], v[122:125], v[106:109], v[82:97]
	v_add_f32_e32 v122, v34, v35
	v_add_f32_e32 v123, v36, v37
	v_add_f32_e32 v122, v122, v123
	v_add_f32_e32 v122, v122, v151
	v_cvt_pk_bf16_f32 v34, v34, v35
	v_cvt_pk_bf16_f32 v35, v36, v37
	ds_read_b64_tr_b16 v[150:151], v162 offset:47104
	ds_read_b64_tr_b16 v[152:153], v162 offset:47616
	v_mfma_f32_32x32x16_bf16 v[66:81], v[118:121], v[106:109], v[66:81]
	v_add_f32_e32 v36, v38, v39
	v_add_f32_e32 v37, v40, v41
	v_add_f32_e32 v36, v36, v37
	v_add_f32_e32 v118, v36, v122
	v_cvt_pk_bf16_f32 v36, v38, v39
	v_cvt_pk_bf16_f32 v37, v40, v41
	ds_read_b64_tr_b16 v[154:155], v162 offset:44032
	ds_read_b64_tr_b16 v[156:157], v162 offset:44544
	s_waitcnt lgkmcnt(13)
	v_mfma_f32_32x32x16_bf16 v[82:97], v[130:133], v[110:113], v[82:97]
	v_add_f32_e32 v38, v42, v43
	v_add_f32_e32 v39, v44, v45
	v_add_f32_e32 v38, v38, v39
	v_add_f32_e32 v40, v38, v118
	v_cvt_pk_bf16_f32 v38, v42, v43
	v_cvt_pk_bf16_f32 v39, v44, v45
	ds_read_b64_tr_b16 v[42:43], v162 offset:48128
	ds_read_b64_tr_b16 v[44:45], v162 offset:48640
	s_waitcnt lgkmcnt(14)
	v_mfma_f32_32x32x16_bf16 v[66:81], v[158:161], v[110:113], v[66:81]
	v_add_f32_e32 v41, v46, v47
	v_add_f32_e32 v118, v48, v49
	v_add_f32_e32 v41, v41, v118
	v_add_f32_e32 v166, v41, v40
	v_cvt_pk_bf16_f32 v40, v46, v47
	v_cvt_pk_bf16_f32 v41, v48, v49
	s_waitcnt lgkmcnt(9)
	v_mfma_f32_32x32x16_bf16 v[82:97], v[126:129], v[114:117], v[82:97]
	s_waitcnt lgkmcnt(8)
	v_mfma_f32_32x32x16_bf16 v[66:81], v[134:137], v[114:117], v[66:81]
	s_add_i32 s61, s44, 2
	s_cmp_lt_i32 s61, s71
	s_cselect_b64 s[52:53], -1, 0
	s_cmp_ge_i32 s61, s71
	s_cselect_b64 s[50:51], -1, 0
	s_cbranch_scc1 .LBB0_1322
	s_xor_b32 s54, s99, 0x5000
	s_add_i32 m0, s54, s66
	s_nop 0
	global_load_lds_dwordx4 v[222:223], off
	s_and_b64 vcc, exec, s[42:43]
	s_cbranch_vccnz .LBB0_1322
	s_add_i32 m0, s54, s70
	s_nop 0
	global_load_lds_dwordx4 v[220:221], off
.LBB0_1322:
	s_lshl_b32 s54, s91, 13
	s_add_i32 m0, s54, s72
	s_nop 0
	global_load_lds_dwordx4 v[218:219], off
	s_cmp_lt_i32 s45, s68
	s_cbranch_scc1 .LBB0_1324
	v_add_u32_e32 v47, 0xffffffa5, v195
	v_add_u32_e32 v46, 0xffffff85, v195
	v_cmp_le_i32_e32 vcc, v47, v191
	s_nop 1
	v_cndmask_b32_e32 v66, v230, v66, vcc
	v_cmp_lt_i32_e32 vcc, v46, v191
	s_nop 1
	v_cndmask_b32_e32 v83, v230, v83, vcc
	v_cmp_le_i32_e32 vcc, v46, v191
	v_add_u32_e32 v46, 0xffffffa6, v195
	s_nop 0
	v_cndmask_b32_e32 v82, v230, v82, vcc
	v_cmp_le_i32_e32 vcc, v46, v191
	v_add_u32_e32 v46, 0xffffff87, v195
	s_nop 0
	v_cndmask_b32_e32 v67, v230, v67, vcc
	v_cmp_le_i32_e32 vcc, v46, v191
	v_add_u32_e32 v46, 0xffffffa7, v195
	s_nop 0
	v_cndmask_b32_e32 v84, v230, v84, vcc
	v_cmp_le_i32_e32 vcc, v46, v191
	v_add_u32_e32 v46, 0xffffff88, v195
	s_nop 0
	v_cndmask_b32_e32 v68, v230, v68, vcc
	v_cmp_le_i32_e32 vcc, v46, v191
	v_add_u32_e32 v46, 0xffffffa8, v195
	s_nop 0
	v_cndmask_b32_e32 v85, v230, v85, vcc
	v_cmp_le_i32_e32 vcc, v46, v191
	v_add_u32_e32 v46, 0xffffff8d, v195
	s_nop 0
	v_cndmask_b32_e32 v69, v230, v69, vcc
	v_cmp_le_i32_e32 vcc, v46, v191
	v_add_u32_e32 v46, 0xffffffad, v195
	s_nop 0
	v_cndmask_b32_e32 v86, v230, v86, vcc
	v_cmp_le_i32_e32 vcc, v46, v191
	v_add_u32_e32 v46, 0xffffff8e, v195
	s_nop 0
	v_cndmask_b32_e32 v70, v230, v70, vcc
	v_cmp_le_i32_e32 vcc, v46, v191
	v_add_u32_e32 v46, 0xffffffae, v195
	s_nop 0
	v_cndmask_b32_e32 v87, v230, v87, vcc
	v_cmp_le_i32_e32 vcc, v46, v191
	v_add_u32_e32 v46, 0xffffff8f, v195
	s_nop 0
	v_cndmask_b32_e32 v71, v230, v71, vcc
	v_cmp_le_i32_e32 vcc, v46, v191
	v_add_u32_e32 v46, 0xffffffaf, v195
	s_nop 0
	v_cndmask_b32_e32 v88, v230, v88, vcc
	v_cmp_le_i32_e32 vcc, v46, v191
	v_add_u32_e32 v46, 0xffffff90, v195
	s_nop 0
	v_cndmask_b32_e32 v72, v230, v72, vcc
	v_cmp_le_i32_e32 vcc, v46, v191
	v_add_u32_e32 v46, 0xffffffb0, v195
	s_nop 0
	v_cndmask_b32_e32 v89, v230, v89, vcc
	v_cmp_le_i32_e32 vcc, v46, v191
	v_add_u32_e32 v46, 0xffffff95, v195
	s_nop 0
	v_cndmask_b32_e32 v73, v230, v73, vcc
	v_cmp_le_i32_e32 vcc, v46, v191
	v_add_u32_e32 v46, 0xffffffb5, v195
	s_nop 0
	v_cndmask_b32_e32 v90, v230, v90, vcc
	v_cmp_le_i32_e32 vcc, v46, v191
	v_add_u32_e32 v46, 0xffffff96, v195
	s_nop 0
	v_cndmask_b32_e32 v74, v230, v74, vcc
	v_cmp_le_i32_e32 vcc, v46, v191
	v_add_u32_e32 v46, 0xffffffb6, v195
	s_nop 0
	v_cndmask_b32_e32 v91, v230, v91, vcc
	v_cmp_le_i32_e32 vcc, v46, v191
	v_add_u32_e32 v46, 0xffffff97, v195
	s_nop 0
	v_cndmask_b32_e32 v75, v230, v75, vcc
	v_cmp_le_i32_e32 vcc, v46, v191
	v_add_u32_e32 v46, 0xffffffb7, v195
	s_nop 0
	v_cndmask_b32_e32 v92, v230, v92, vcc
	v_cmp_le_i32_e32 vcc, v46, v191
	v_add_u32_e32 v46, 0xffffff98, v195
	s_nop 0
	v_cndmask_b32_e32 v76, v230, v76, vcc
	v_cmp_le_i32_e32 vcc, v46, v191
	v_add_u32_e32 v46, 0xffffffb8, v195
	s_nop 0
	v_cndmask_b32_e32 v93, v230, v93, vcc
	v_cmp_le_i32_e32 vcc, v46, v191
	v_add_u32_e32 v46, 0xffffff9d, v195
	s_nop 0
	v_cndmask_b32_e32 v77, v230, v77, vcc
	v_cmp_le_i32_e32 vcc, v46, v191
	v_add_u32_e32 v46, 0xffffffbd, v195
	s_nop 0
	v_cndmask_b32_e32 v94, v230, v94, vcc
	v_cmp_le_i32_e32 vcc, v46, v191
	v_add_u32_e32 v46, 0xffffff9e, v195
	s_nop 0
	v_cndmask_b32_e32 v78, v230, v78, vcc
	v_cmp_le_i32_e32 vcc, v46, v191
	v_add_u32_e32 v46, 0xffffffbe, v195
	s_nop 0
	v_cndmask_b32_e32 v95, v230, v95, vcc
	v_cmp_le_i32_e32 vcc, v46, v191
	v_add_u32_e32 v46, 0xffffff9f, v195
	s_nop 0
	v_cndmask_b32_e32 v79, v230, v79, vcc
	v_cmp_le_i32_e32 vcc, v46, v191
	v_add_u32_e32 v46, 0xffffffbf, v195
	s_nop 0
	v_cndmask_b32_e32 v96, v230, v96, vcc
	v_cmp_le_i32_e32 vcc, v46, v191
	v_add_u32_e32 v46, 0xffffffa0, v195
	s_nop 0
	v_cndmask_b32_e32 v80, v230, v80, vcc
	v_cmp_le_i32_e32 vcc, v46, v191
	v_subrev_u32_e32 v46, 64, v195
	s_nop 0
	v_cndmask_b32_e32 v97, v230, v97, vcc
	v_cmp_le_i32_e32 vcc, v46, v191
	s_nop 1
	v_cndmask_b32_e32 v81, v230, v81, vcc

.LBB0_1331:
	v_mfma_f32_32x32x16_bf16 v[50:65], v[138:141], v[98:101], 0
	v_lshl_add_u32 v199, s92, 13, v240
	ds_read_b64_tr_b16 v[162:163], v199 offset:40960
	ds_read_b64_tr_b16 v[164:165], v199 offset:41472
	s_waitcnt lgkmcnt(7)
	v_add_f32_e32 v34, v82, v83
	v_add_f32_e32 v35, v84, v85
	v_add_f32_e32 v34, v34, v35
	v_cvt_pk_bf16_f32 v154, v82, v83
	v_cvt_pk_bf16_f32 v155, v84, v85
	ds_read_b64_tr_b16 v[158:159], v199 offset:45056
	ds_read_b64_tr_b16 v[160:161], v199 offset:45568
	v_add_f32_e32 v35, v86, v87
	v_add_f32_e32 v36, v88, v89
	v_add_f32_e32 v35, v35, v36
	v_add_f32_e32 v82, v35, v34
	s_waitcnt lgkmcnt(8)
	v_mfma_f32_32x32x16_bf16 v[34:49], v[130:133], v[98:101], 0
	v_cvt_pk_bf16_f32 v156, v86, v87
	v_cvt_pk_bf16_f32 v157, v88, v89
	ds_read_b128 v[170:173], v197 offset:6144
	ds_read_b128 v[174:177], v197 offset:6656
	ds_read_b64_tr_b16 v[150:151], v199 offset:41984
	ds_read_b64_tr_b16 v[152:153], v199 offset:42496
	s_waitcnt lgkmcnt(11)
	v_mfma_f32_32x32x16_bf16 v[50:65], v[134:137], v[102:105], v[50:65]
	v_add_f32_e32 v83, v90, v91
	v_add_f32_e32 v84, v92, v93
	v_add_f32_e32 v83, v83, v84
	v_add_f32_e32 v82, v83, v82
	v_cvt_pk_bf16_f32 v142, v90, v91
	v_cvt_pk_bf16_f32 v143, v92, v93
	ds_read_b64_tr_b16 v[146:147], v199 offset:46080
	ds_read_b64_tr_b16 v[148:149], v199 offset:46592
	s_waitcnt lgkmcnt(12)
	v_mfma_f32_32x32x16_bf16 v[34:49], v[126:129], v[102:105], v[34:49]
	v_add_f32_e32 v83, v94, v95
	v_add_f32_e32 v84, v96, v97
	v_add_f32_e32 v83, v83, v84
	v_add_f32_e32 v82, v83, v82
	v_cvt_pk_bf16_f32 v144, v94, v95
	v_cvt_pk_bf16_f32 v145, v96, v97
	ds_read_b128 v[248:251], v197 offset:8192
	ds_read_b128 v[232:235], v197 offset:8704
	ds_read_b64_tr_b16 v[90:91], v199 offset:43008
	ds_read_b64_tr_b16 v[92:93], v199 offset:43520
	s_waitcnt lgkmcnt(14)
	v_mfma_f32_32x32x16_bf16 v[50:65], v[122:125], v[106:109], v[50:65]
	v_add_f32_e32 v83, v66, v67
	v_add_f32_e32 v84, v68, v69
	v_add_f32_e32 v83, v83, v84
	v_add_f32_e32 v84, v83, v82
	v_cvt_pk_bf16_f32 v82, v66, v67
	v_cvt_pk_bf16_f32 v83, v68, v69
	ds_read_b64_tr_b16 v[86:87], v199 offset:47104
	ds_read_b64_tr_b16 v[88:89], v199 offset:47616
	v_mfma_f32_32x32x16_bf16 v[34:49], v[118:121], v[106:109], v[34:49]
	v_add_f32_e32 v66, v70, v71
	v_add_f32_e32 v67, v72, v73
	v_add_f32_e32 v66, v66, v67
	v_add_f32_e32 v66, v66, v84
	v_cvt_pk_bf16_f32 v84, v70, v71
	v_cvt_pk_bf16_f32 v85, v72, v73
	ds_read_b64_tr_b16 v[70:71], v199 offset:44032
	ds_read_b64_tr_b16 v[72:73], v199 offset:44544
	s_waitcnt lgkmcnt(13)
	v_mfma_f32_32x32x16_bf16 v[50:65], v[170:173], v[110:113], v[50:65]
	v_add_f32_e32 v67, v74, v75
	v_add_f32_e32 v68, v76, v77
	v_add_f32_e32 v67, v67, v68
	v_add_f32_e32 v68, v67, v66
	v_cvt_pk_bf16_f32 v66, v74, v75
	v_cvt_pk_bf16_f32 v67, v76, v77
	ds_read_b64_tr_b16 v[74:75], v199 offset:48128
	ds_read_b64_tr_b16 v[76:77], v199 offset:48640
	s_waitcnt lgkmcnt(14)
	v_mfma_f32_32x32x16_bf16 v[34:49], v[174:177], v[110:113], v[34:49]
	v_add_f32_e32 v69, v78, v79
	v_add_f32_e32 v94, v80, v81
	v_add_f32_e32 v69, v69, v94
	v_add_f32_e32 v94, v69, v68
	v_cvt_pk_bf16_f32 v68, v78, v79
	v_cvt_pk_bf16_f32 v69, v80, v81
	s_waitcnt lgkmcnt(9)
	v_mfma_f32_32x32x16_bf16 v[50:65], v[248:251], v[114:117], v[50:65]
	s_waitcnt lgkmcnt(8)
	v_mfma_f32_32x32x16_bf16 v[34:49], v[232:235], v[114:117], v[34:49]
	s_add_i32 s54, s44, 3
	s_cmp_lt_i32 s54, s71
	s_cselect_b64 s[52:53], -1, 0
	s_cbranch_scc0 .LBB0_1334
	s_ashr_i32 s55, s54, 31
	s_lshl_b64 s[58:59], s[54:55], 17
	s_add_i32 m0, s98, s66
	v_lshl_add_u64 v[78:79], v[212:213], 0, s[58:59]
	global_load_lds_dwordx4 v[78:79], off
	s_and_b64 vcc, exec, s[42:43]
	s_cbranch_vccnz .LBB0_1334
	s_lshl_b64 s[54:55], s[54:55], 11
	s_add_i32 m0, s98, s70
	v_lshl_add_u64 v[78:79], v[214:215], 0, s[54:55]
	global_load_lds_dwordx4 v[78:79], off
.LBB0_1334:
	s_add_i32 s54, s44, 1
	s_xor_b32 s93, s98, 0x5000
	s_cmp_lt_i32 s54, s71
	s_cselect_b64 s[58:59], -1, 0
	s_cbranch_scc0 .LBB0_1336
	s_ashr_i32 s55, s54, 31
	s_lshl_b64 s[62:63], s[54:55], 17
	s_lshl_b32 s45, s90, 13
	s_add_i32 m0, s45, s72
	v_lshl_add_u64 v[78:79], v[216:217], 0, s[62:63]
	global_load_lds_dwordx4 v[78:79], off
